# P14 rewrite + static s_setprio 1 for waves 4-7 during the attention loops
# baseline (speedup 1.0000x reference)
; #define LAS __attribute__((address_space(3)))
; __device__ __forceinline__ int v_rd_base(int lane) { return ((lane & 3) << 3) | (((lane >> 2) & 3) << 6) | (((lane >> 4) & 1) << 5) | (((lane >> 5) & 1) << 8); }
; template <int MODE>
; __device__ __forceinline__ void attn_unit(const bf16* __restrict__ qkv, bf16* __restrict__ O, const float* __restrict__ kmean, int b, int h, int qb, LAS unsigned char* ldsl, LAS unsigned char* lepi, int wid) {
;     const int lane = (int)__builtin_amdgcn_mbcnt_hi(~0u, __builtin_amdgcn_mbcnt_lo(~0u, 0u)), tid = wid * 64 + lane, r32 = lane & 31, hi = lane >> 5;
;     const size_t rowbase = (size_t)b * SEQ;
;     const bf16* Qp = qkv + (MODE == 0 ? 0 : 3 * 1024) + h * HD;
;     const bf16* Kp = Qp + 1024 + rowbase * PITCH; const bf16* Vp = Qp + 2048 + rowbase * PITCH;
;     LAS const unsigned char* K_lds = ldsl + 2 * SHM_V;
;     LAS float* ws = (LAS float*)(lepi + EPI_WS) + wid * 64; LAS float* li_l = ws; LAS float* al_l = ws + 32;
;     volatile LAS int* flags = (volatile LAS int*)(lepi + EPI_FLAG);
;     LAS unsigned char* q_lds = ldsl + LDS_Q + wid * 8192 + lane * 16;
;     const int qlo = qb * 256 + wid * 32, qpos = qlo + r32;
; #pragma unroll
;     for (int d0 = 0; d0 < 8; ++d0) *(LAS bf16x8*)(q_lds + d0 * 1024) = *(const bf16x8*)(Qp + (rowbase + qpos) * PITCH + d0 * 16 + hi * 8);
;     const int NT = 4 * (qb + 1);
;     const int vb0 = (int)(unsigned)(uintptr_t)ldsl + v_rd_base(lane);
;     unsigned koff0, koff1, voff0, voff1;
;     { const int b0 = tid * 16, b1 = b0 + 8192;
;       { const int row = b0 >> 8, cb = b0 & 255, colB = cb ^ ((row & 7) << 4); koff0 = (unsigned)(row * PITCH + (colB >> 1)) * 2u; }
;       { const int row = b1 >> 8, cb = b1 & 255, colB = cb ^ ((row & 7) << 4); koff1 = (unsigned)(row * PITCH + (colB >> 1)) * 2u; }
;       { const int st = b0 >> 9, wb = b0 & 511, kk = (st >> 2) * 8 + (wb >> 6), c = (st & 3) * 32 + ((wb & 63) >> 1), k = (kk & ~0xC) | ((kk & 4) << 1) | ((kk & 8) >> 1); voff0 = (unsigned)(k * PITCH + c) * 2u; }
;       { const int st = b1 >> 9, wb = b1 & 511, kk = (st >> 2) * 8 + (wb >> 6), c = (st & 3) * 32 + ((wb & 63) >> 1), k = (kk & ~0xC) | ((kk & 4) << 1) | ((kk & 8) >> 1); voff1 = (unsigned)(k * PITCH + c) * 2u; } }
;     const unsigned ldsw = (unsigned)wid * 1024u;
.LBB0_580:
	v_readlane_b32 s0, v254, 37
	v_readlane_b32 s1, v254, 38
	s_andn2_b64 vcc, exec, s[0:1]
	s_cbranch_vccnz .LBB0_942
	s_cmp_lt_u32 s85, 4
	s_cbranch_scc1 .Lattn_prio_skip
	s_setprio 1
.Lattn_prio_skip:
	v_writelane_b32 v254, s72, 56
	v_writelane_b32 v254, s71, 57
	v_writelane_b32 v254, s70, 58
	v_writelane_b32 v254, s69, 59
	v_writelane_b32 v254, s68, 60
	v_writelane_b32 v254, s65, 61
	v_writelane_b32 v254, s96, 62
	v_writelane_b32 v254, s94, 63
	s_waitcnt vmcnt(0)
	v_lshlrev_b32_e32 v133, 4, v202
	v_lshlrev_b32_e32 v2, 3, v202
	v_writelane_b32 v255, s95, 0
	v_writelane_b32 v255, s90, 1
	s_lshl_b32 s0, s91, 2
	s_add_i32 s96, s0, 0
	s_lshl_b32 s0, s85, 13
	v_and_b32_e32 v3, 0xc0, v133
	v_lshlrev_b32_e32 v5, 1, v202
	s_add_i32 s0, s0, 0
	v_add_u32_e32 v0, s91, v202
	v_and_or_b32 v3, v2, 24, v3
	v_and_b32_e32 v5, 32, v5
	v_and_b32_e32 v2, 0x100, v2
	s_add_i32 s0, s0, 0x10000
	v_or3_b32 v5, v3, v5, v2
	v_lshlrev_b32_e32 v2, 4, v0
	v_add_u32_e32 v204, s0, v133
	v_add_u32_e32 v3, 0x2000, v2
	v_ashrrev_i32_e32 v6, 4, v0
	s_movk_i32 s0, 0x3000
	v_and_b32_e32 v2, 0xf0, v2
	v_and_b32_e32 v7, 0x70, v0
	v_mul_lo_u32 v8, v6, s0
	v_ashrrev_i32_e32 v3, 8, v3
	v_bitop3_b32 v134, v2, v8, v7 bitop3:0xde
	v_lshlrev_b32_e32 v7, 4, v3
	v_and_b32_e32 v7, 0x70, v7
	v_mul_i32_i24_e32 v8, 0x3000, v3
	v_bitop3_b32 v136, v7, v8, v2 bitop3:0xde
	v_bfe_u32 v7, v0, 2, 2
	v_and_b32_e32 v8, 0x60, v0
	v_lshlrev_b32_e32 v2, 3, v0
	v_lshrrev_b32_e32 v0, 1, v0
	v_and_b32_e32 v11, 8, v0
	v_lshrrev_b32_e32 v0, 1, v6
	v_and_b32_e32 v10, -16, v6
	v_and_b32_e32 v6, 4, v0
	v_writelane_b32 v255, s91, 2
	v_or_b32_e32 v0, v6, v10
	v_writelane_b32 v255, s85, 3
	v_and_b32_e32 v9, 24, v2
	v_or3_b32 v0, v0, v7, v11
	s_movk_i32 s3, 0x1800
	v_writelane_b32 v255, s66, 4
	s_load_dwordx2 s[4:5], s[66:67], 0xe0
	v_or_b32_e32 v2, v9, v8
	v_mul_lo_u32 v0, v0, s3
	v_or_b32_e32 v0, v0, v2
	v_lshlrev_b32_e32 v138, 1, v0
	v_lshrrev_b32_e32 v0, 1, v3
	v_and_b32_e32 v0, 4, v0
	s_mov_b32 s0, 0xfffff0
	s_add_i32 s96, s96, 0x20000
	v_and_or_b32 v0, v3, s0, v0
	v_writelane_b32 v255, s67, 5
	s_waitcnt lgkmcnt(0)
	s_add_u32 s1, s4, 0x41001800
	v_or3_b32 v0, v0, v7, v11
	v_writelane_b32 v255, s1, 6
	s_addc_u32 s1, s5, 0
	v_mul_i32_i24_e32 v12, 0x1800, v0
	v_writelane_b32 v255, s1, 8
	v_or_b32_e32 v0, v12, v2
	v_lshrrev_b32_e32 v4, 5, v202
	v_mov_b32_e32 v1, 0
	v_writelane_b32 v255, s91, 9
	v_lshlrev_b32_e32 v140, 1, v0
	v_and_b32_e32 v0, 0x60, v202
	v_writelane_b32 v255, s4, 10
	s_mov_b64 s[0:1], 0x290000
	v_lshlrev_b32_e32 v197, 4, v4
	v_lshl_add_u64 v[2:3], s[4:5], 0, v[0:1]
	s_movk_i32 s2, 0x70
	v_lshl_add_u64 v[142:143], v[2:3], 0, s[0:1]
	v_add_u32_e32 v2, 32, v197
	v_and_b32_e32 v3, 64, v202
	v_bitop3_b32 v208, v2, v133, s2 bitop3:0x78
	v_xor_b32_e32 v2, 1, v202
	v_add_u32_e32 v3, 64, v3
	v_lshlrev_b32_e32 v98, 14, v4
	v_mov_b32_e32 v99, v1
	s_mov_b64 s[0:1], 0x8000
	v_cmp_lt_i32_e32 vcc, v2, v3
	v_lshl_add_u64 v[106:107], v[98:99], 0, s[0:1]
	s_mov_b64 s[0:1], 0x9000
	v_cndmask_b32_e32 v2, v202, v2, vcc
	v_lshl_add_u64 v[108:109], v[98:99], 0, s[0:1]
	s_mov_b64 s[0:1], 0xa000
	v_lshlrev_b32_e32 v211, 2, v2
	v_and_b32_e32 v2, 1, v202
	v_lshl_add_u64 v[110:111], v[98:99], 0, s[0:1]
	s_mov_b64 s[0:1], 0xb000
	v_cmp_eq_u32_e64 s[8:9], 0, v2
	v_lshl_add_u64 v[112:113], v[98:99], 0, s[0:1]
	s_mov_b64 s[0:1], 0x18000
	v_or_b32_e32 v2, v10, v11
	v_lshl_add_u64 v[122:123], v[98:99], 0, s[0:1]
	s_mov_b64 s[0:1], 0x19000
	v_or3_b32 v2, v2, v6, v7
	v_lshl_add_u64 v[124:125], v[98:99], 0, s[0:1]
	s_mov_b64 s[0:1], 0x1a000
	v_mul_lo_u32 v2, v2, s3
	v_and_b32_e32 v0, 0x70, v133
	v_lshl_add_u64 v[126:127], v[98:99], 0, s[0:1]
	s_mov_b64 s[0:1], 0x1b000
	v_or3_b32 v2, v2, v8, v9
	v_and_b32_e32 v203, 31, v202
	v_bitop3_b32 v209, v197, v0, 64 bitop3:0x36
	v_add_u32_e32 v0, 0x60, v197
	v_lshl_add_u64 v[128:129], v[98:99], 0, s[0:1]
	v_lshlrev_b32_e32 v144, 1, v2
	v_or3_b32 v2, v12, v8, v9
	v_readlane_b32 s0, v254, 39
	v_writelane_b32 v255, s5, 11
	v_bitop3_b32 v210, v0, v133, s2 bitop3:0x78
	v_lshlrev_b32_e32 v0, 2, v4
	v_lshlrev_b32_e32 v146, 1, v2
	v_add_u32_e32 v2, s0, v203
	v_lshlrev_b32_e32 v132, 3, v4
	v_mov_b32_e32 v139, v1
	v_mov_b32_e32 v141, v1
	v_mov_b32_e32 v135, v1
	v_mov_b32_e32 v137, v1
	v_add_u32_e32 v205, 0, v5
	v_lshl_add_u32 v206, v203, 8, 0
	v_bitop3_b32 v207, v133, v197, s2 bitop3:0x6c
	v_cmp_gt_u32_e64 s[6:7], 32, v202
	v_lshl_add_u32 v198, v203, 2, s96
	v_or_b32_e32 v100, 0x1000, v98
	v_mov_b32_e32 v101, v1
	v_or_b32_e32 v102, 0x2000, v98
	v_mov_b32_e32 v103, v1
	v_or_b32_e32 v104, 0x3000, v98
	v_mov_b32_e32 v105, v1
	v_or_b32_e32 v114, 0x10000, v98
	v_mov_b32_e32 v115, v1
	v_or_b32_e32 v116, 0x11000, v98
	v_mov_b32_e32 v117, v1
	v_or_b32_e32 v118, 0x12000, v98
	v_mov_b32_e32 v119, v1
	v_or_b32_e32 v120, 0x13000, v98
	v_mov_b32_e32 v121, v1
	v_mov_b32_e32 v145, v1
	v_mov_b32_e32 v147, v1
	v_sub_u32_e32 v196, v2, v0
	s_mov_b64 s[2:3], 0x410c2800
	s_mov_b64 s[4:5], 0x410c2000
	s_mov_b32 s84, 0x41000000
	s_mov_b64 s[42:43], 0x41182800
	s_mov_b64 s[88:89], 0x41182000
	v_mov_b32_e32 v199, 0xff800000
	v_writelane_b32 v255, s93, 12
	s_branch .LBB0_583

; __global__ void __launch_bounds__(NTHR, 2) fwd_kernel(Args args) {
;     ...
;         for (int p = wg; p < 256; p += G) { const int bh = p >> 3, k = p & 7, b = bh >> 3, h = bh & 7;
;             for (int s = 0; s < 2; ++s) att::attn_unit<1>(QKV, OB, kmean, b, h, s ? 15 - k : k, ring, lepi, wave_s); }
;         for (int p = wg; p < 256; p += G) { const int bh = p >> 3, k = p & 7, b = bh >> 3, h = bh & 7;
;             for (int s = 0; s < 2; ++s) att::attn_unit<0>(QKV, OB, kmean, b, h, s ? 15 - k : k, ring, lepi, wave_s); }
;     ...
;         }
;     ...
;         if (half == 0) { __syncthreads(); CONVERT_RANGE(0, NEXP_ITEMS); }
.LBB0_941:
	s_setprio 0
	v_readlane_b32 s94, v254, 63
	v_readlane_b32 s95, v255, 0
	s_load_dword s92, s[94:95], 0xf0
	v_readlane_b32 s90, v255, 1
	v_readlane_b32 s91, v255, 2
	v_readlane_b32 s66, v255, 4
	v_readlane_b32 s93, v255, 12
	v_readlane_b32 s96, v254, 62
	v_readlane_b32 s91, v255, 9
	v_readlane_b32 s77, v254, 32
	v_readlane_b32 s80, v254, 33
	v_readlane_b32 s81, v254, 34
	v_readlane_b32 s85, v255, 3
	v_readlane_b32 s67, v255, 5
	v_readlane_b32 s65, v254, 61
	v_readlane_b32 s68, v254, 60
	v_readlane_b32 s69, v254, 59
	v_readlane_b32 s70, v254, 58
	v_readlane_b32 s71, v254, 57
	v_readlane_b32 s72, v254, 56
